# alignment barrier of wave group 0 deferred to the epilogue head in the two MoE GEMM phases (P8, P9)
# speedup vs baseline: 1.0047x; 1.0047x over previous
; #define LAS __attribute__((address_space(3)))
;     __device__ __forceinline__ bool next(int i, pg8::Unit& u) const { const int L = i * G + c; if (L >= nM * 4) return false; int pm, pn; pg8::tile_remap<4>(L, nM, pm, pn); if (rev) pm = nM - 1 - pm; u.pm = pm; u.pn = pn; u.aux = 0; u.skip = 0; return true; }
;     __device__ __forceinline__ bool next(int i, pg8::Unit& u) const { const int L = first + i * stride; if (i >= nmine || L >= 512) return false; u.pm = L & 3; u.pn = (L >> 2) & 3; u.aux = L >> 4; u.skip = 0; return true; }
;     __device__ __forceinline__ bool next(int i, pg8::Unit& u) const { if (!TW) { const bool r = Base::next(i, u); u.skip = 0; return r; } const bool r = Base::next(i >> 1, u); u.skip = !(i & 1); return r; }
;     const int nwg = nM * NN; int wgid = L;
;     { const int q = nwg >> 3, r = nwg & 7, xcd = wgid & 7, off = wgid >> 3; wgid = (xcd < r ? xcd * (q + 1) : r * (q + 1) + (xcd - r) * q) + off; }
;     constexpr int nig = WGM * NN; const int gid = wgid / nig, idx = wgid - gid * nig, fm = gid * WGM, left = nM - fm;
;     if (left >= WGM) { pm = fm + (idx % WGM); pn = idx / WGM; } else { pm = fm + (idx % left); pn = idx / left; }
; }
;     __device__ __forceinline__ bool next(int i, pg8::Unit& u) const {
;         const int L = i * G + c; if (L >= NT * NN) return false; pg8::tile_remap<NN>(L, NT, u.pm, u.pn);
;         if (!GATH) u.pm = NT - 1 - u.pm;
;         u.aux = __builtin_amdgcn_readfirstlane((int)((const LAS unsigned char*)tpre + 11264)[u.pm]); u.skip = 0; return true; }
.LBB0_1065:
.LBB0_1067:
	v_cndmask_b32_e64 v2, 0, 1, s[10:11]
	v_cmp_ne_u32_e64 s[2:3], 1, v2
	s_andn2_b64 vcc, exec, s[10:11]
	s_cbranch_vccnz .LBB0_1074
	s_add_i32 s10, s48, 2
	s_mul_i32 s25, s10, s92
	s_add_i32 s25, s25, s33
	s_cmp_ge_i32 s25, s40
	s_mov_b64 s[10:11], 0
	s_cbranch_scc1 .LBB0_1075
	s_and_b32 s5, s25, 7
	s_cmp_ge_u32 s5, s64
	s_mov_b64 s[10:11], -1
	s_cbranch_scc0 .LBB0_1071
	s_sub_i32 s10, s5, s64
	s_mul_i32 s10, s10, s63
	s_add_i32 s14, s10, s66
	s_mov_b64 s[10:11], 0

; #define LAS __attribute__((address_space(3)))
; __device__ __forceinline__ unsigned pk4_fp8(float a, float b, float c, float d) { int w = __builtin_amdgcn_cvt_pk_fp8_f32(a, b, 0, false); w = __builtin_amdgcn_cvt_pk_fp8_f32(c, d, w, true); return (unsigned)w; }
;     __device__ __forceinline__ void operator()(const f32x4 (&acc)[2][2][4][2], const pg8::Unit& u, int wr, int wc, int fr, int fq) const {
;         const int col0 = u.pn * 256 + wc * 64 + 16 * fq;
;         unsigned char* Yt = ws + WS_Y + (size_t)u.pm * TSF8;
;         f32x4 bd[2][2];
; #pragma unroll
;         for (int bj = 0; bj < 2; ++bj) { const LAS float* bt = (const LAS float*)(btab + u.par * 1024) + wc * 64 + 16 * fq + bj * 8; bd[bj][0] = *(const LAS f32x4*)bt; bd[bj][1] = *(const LAS f32x4*)(bt + 4); }
; #pragma unroll
;         for (int ai = 0; ai < 2; ++ai)
; #pragma unroll
;             for (int m = 0; m < 4; ++m) { const int rl = ai * 128 + wr * 64 + m * 16 + fr;
;                 { const f32x4 v0 = acc[ai][0][m][0] * (1.0f / 64.0f) + bd[0][0], v1 = acc[ai][0][m][1] * (1.0f / 64.0f) + bd[0][1], v2 = acc[ai][1][m][0] * (1.0f / 64.0f) + bd[1][0], v3 = acc[ai][1][m][1] * (1.0f / 64.0f) + bd[1][1];
;                     *(u32x4*)(Yt + (size_t)rl * D + col0) = (u32x4){pk4_fp8(v0[0], v0[1], v0[2], v0[3]), pk4_fp8(v1[0], v1[1], v1[2], v1[3]), pk4_fp8(v2[0], v2[1], v2[2], v2[3]), pk4_fp8(v3[0], v3[1], v3[2], v3[3])}; } }
.LBB0_1074:
	s_mov_b64 s[10:11], 0
.LBB0_1075:
	s_and_b64 vcc, exec, s[18:19]
	s_cbranch_vccz .Lmy_nobar1
	s_barrier
.Lmy_nobar1:
	v_mov_b32_e32 v19, v0
	s_lshl_b32 s15, s15, 8
	s_or_b32 s15, s15, s61
	v_and_b32_e32 v2, 48, v19
	v_or_b32_e32 v18, s15, v2
	s_add_i32 s15, s62, s70
	v_lshl_add_u32 v2, v2, 2, s15
	ds_read_b128 v[14:17], v2
	ds_read_b128 v[10:13], v2 offset:16
	ds_read_b128 v[6:9], v2 offset:32
	ds_read_b128 v[2:5], v2 offset:48
	v_mov_b32_e32 v20, 0
	s_waitcnt lgkmcnt(3)
	v_pk_fma_f32 v[22:23], v[150:151], s[22:23], v[14:15] op_sel_hi:[1,0,1]
	s_ashr_i32 s25, s24, 31
	s_waitcnt lgkmcnt(2)
	v_pk_fma_f32 v[30:31], v[146:147], s[22:23], v[10:11] op_sel_hi:[1,0,1]
	s_waitcnt lgkmcnt(1)
	v_pk_fma_f32 v[146:147], v[158:159], s[22:23], v[6:7] op_sel_hi:[1,0,1]
	s_waitcnt lgkmcnt(0)
	v_pk_fma_f32 v[150:151], v[154:155], s[22:23], v[2:3] op_sel_hi:[1,0,1]
	v_cvt_pk_fp8_f32 v20, v22, v23
	v_mov_b32_e32 v21, 0
	v_mov_b32_e32 v22, 0
	v_mov_b32_e32 v23, 0
	s_lshl_b64 s[24:25], s[24:25], 18
	v_cvt_pk_fp8_f32 v21, v30, v31
	v_cvt_pk_fp8_f32 v22, v146, v147
	v_cvt_pk_fp8_f32 v23, v150, v151
	s_add_u32 s24, s50, s24
	s_addc_u32 s25, s51, s25
	v_and_or_b32 v24, v19, 15, s49
	v_ashrrev_i32_e32 v19, 31, v18
	v_lshl_add_u64 v[26:27], s[24:25], 0, v[18:19]
	v_pk_fma_f32 v[18:19], v[152:153], s[22:23], v[16:17] op_sel_hi:[1,0,1]
	v_pk_fma_f32 v[28:29], v[148:149], s[22:23], v[12:13] op_sel_hi:[1,0,1]
	v_pk_fma_f32 v[32:33], v[160:161], s[22:23], v[8:9] op_sel_hi:[1,0,1]
	v_pk_fma_f32 v[148:149], v[156:157], s[22:23], v[4:5] op_sel_hi:[1,0,1]
	v_cvt_pk_fp8_f32 v20, v18, v19 op_sel:[0,0,1]
	v_cvt_pk_fp8_f32 v21, v28, v29 op_sel:[0,0,1]
	v_cvt_pk_fp8_f32 v22, v32, v33 op_sel:[0,0,1]
	v_cvt_pk_fp8_f32 v23, v148, v149 op_sel:[0,0,1]
	v_ashrrev_i32_e32 v25, 31, v24
	v_lshlrev_b64 v[18:19], 10, v[24:25]
	v_lshl_add_u64 v[18:19], v[26:27], 0, v[18:19]
	global_store_dwordx4 v[18:19], v[20:23], off
	v_pk_fma_f32 v[130:131], v[130:131], s[22:23], v[10:11] op_sel_hi:[1,0,1]
	v_pk_fma_f32 v[138:139], v[138:139], s[22:23], v[2:3] op_sel_hi:[1,0,1]
	v_pk_fma_f32 v[22:23], v[134:135], s[22:23], v[14:15] op_sel_hi:[1,0,1]
	v_mov_b32_e32 v20, 0
	v_pk_fma_f32 v[134:135], v[142:143], s[22:23], v[6:7] op_sel_hi:[1,0,1]
	v_cvt_pk_fp8_f32 v20, v22, v23
	v_mov_b32_e32 v21, 0
	v_mov_b32_e32 v22, 0
	v_mov_b32_e32 v23, 0
	v_cvt_pk_fp8_f32 v21, v130, v131
	v_cvt_pk_fp8_f32 v22, v134, v135
	v_cvt_pk_fp8_f32 v23, v138, v139
	v_pk_fma_f32 v[30:31], v[136:137], s[22:23], v[16:17] op_sel_hi:[1,0,1]
	v_pk_fma_f32 v[32:33], v[132:133], s[22:23], v[12:13] op_sel_hi:[1,0,1]
	v_pk_fma_f32 v[132:133], v[144:145], s[22:23], v[8:9] op_sel_hi:[1,0,1]
	v_pk_fma_f32 v[136:137], v[140:141], s[22:23], v[4:5] op_sel_hi:[1,0,1]
	v_or_b32_e32 v28, 16, v24
	v_cvt_pk_fp8_f32 v20, v30, v31 op_sel:[0,0,1]
	v_cvt_pk_fp8_f32 v21, v32, v33 op_sel:[0,0,1]
	v_cvt_pk_fp8_f32 v22, v132, v133 op_sel:[0,0,1]
	v_cvt_pk_fp8_f32 v23, v136, v137 op_sel:[0,0,1]
	v_ashrrev_i32_e32 v29, 31, v28
	v_lshlrev_b64 v[28:29], 10, v[28:29]
	v_lshl_add_u64 v[28:29], v[26:27], 0, v[28:29]
	global_store_dwordx4 v[28:29], v[20:23], off
	v_pk_fma_f32 v[114:115], v[114:115], s[22:23], v[10:11] op_sel_hi:[1,0,1]
	v_pk_fma_f32 v[122:123], v[122:123], s[22:23], v[2:3] op_sel_hi:[1,0,1]
	v_pk_fma_f32 v[22:23], v[118:119], s[22:23], v[14:15] op_sel_hi:[1,0,1]
	v_mov_b32_e32 v20, 0
	v_pk_fma_f32 v[118:119], v[126:127], s[22:23], v[6:7] op_sel_hi:[1,0,1]
	v_cvt_pk_fp8_f32 v20, v22, v23
	v_mov_b32_e32 v21, 0
	v_mov_b32_e32 v22, 0
	v_mov_b32_e32 v23, 0
	v_cvt_pk_fp8_f32 v21, v114, v115
	v_cvt_pk_fp8_f32 v22, v118, v119
	v_cvt_pk_fp8_f32 v23, v122, v123
	v_pk_fma_f32 v[30:31], v[120:121], s[22:23], v[16:17] op_sel_hi:[1,0,1]
	v_pk_fma_f32 v[32:33], v[116:117], s[22:23], v[12:13] op_sel_hi:[1,0,1]
	v_pk_fma_f32 v[116:117], v[128:129], s[22:23], v[8:9] op_sel_hi:[1,0,1]
	v_pk_fma_f32 v[120:121], v[124:125], s[22:23], v[4:5] op_sel_hi:[1,0,1]
	v_or_b32_e32 v28, 32, v24
	v_cvt_pk_fp8_f32 v20, v30, v31 op_sel:[0,0,1]
	v_cvt_pk_fp8_f32 v21, v32, v33 op_sel:[0,0,1]
	v_cvt_pk_fp8_f32 v22, v116, v117 op_sel:[0,0,1]
	v_cvt_pk_fp8_f32 v23, v120, v121 op_sel:[0,0,1]
	v_ashrrev_i32_e32 v29, 31, v28
	v_lshlrev_b64 v[28:29], 10, v[28:29]
	v_lshl_add_u64 v[28:29], v[26:27], 0, v[28:29]
	global_store_dwordx4 v[28:29], v[20:23], off
	v_pk_fma_f32 v[28:29], v[104:105], s[22:23], v[16:17] op_sel_hi:[1,0,1]
	v_pk_fma_f32 v[30:31], v[100:101], s[22:23], v[12:13] op_sel_hi:[1,0,1]
	v_pk_fma_f32 v[22:23], v[102:103], s[22:23], v[14:15] op_sel_hi:[1,0,1]
	v_mov_b32_e32 v20, 0
	v_pk_fma_f32 v[32:33], v[98:99], s[22:23], v[10:11] op_sel_hi:[1,0,1]
	v_pk_fma_f32 v[100:101], v[110:111], s[22:23], v[6:7] op_sel_hi:[1,0,1]
	v_pk_fma_f32 v[104:105], v[106:107], s[22:23], v[2:3] op_sel_hi:[1,0,1]
	v_cvt_pk_fp8_f32 v20, v22, v23
	v_mov_b32_e32 v21, 0
	v_mov_b32_e32 v22, 0
	v_mov_b32_e32 v23, 0
	v_cvt_pk_fp8_f32 v21, v32, v33
	v_cvt_pk_fp8_f32 v22, v100, v101
	v_cvt_pk_fp8_f32 v23, v104, v105
	v_pk_fma_f32 v[98:99], v[112:113], s[22:23], v[8:9] op_sel_hi:[1,0,1]
	v_pk_fma_f32 v[102:103], v[108:109], s[22:23], v[4:5] op_sel_hi:[1,0,1]
	v_or_b32_e32 v24, 48, v24
	v_cvt_pk_fp8_f32 v20, v28, v29 op_sel:[0,0,1]
; __device__ __forceinline__ unsigned pk4_fp8(float a, float b, float c, float d) { int w = __builtin_amdgcn_cvt_pk_fp8_f32(a, b, 0, false); w = __builtin_amdgcn_cvt_pk_fp8_f32(c, d, w, true); return (unsigned)w; }
; #define PG8_UNI64(p) ((const char*)((((unsigned long long)(unsigned)__builtin_amdgcn_readfirstlane((int)((unsigned long long)(p) >> 32))) << 32) | (unsigned long long)(unsigned)__builtin_amdgcn_readfirstlane((int)(unsigned)(unsigned long long)(p))))
;     __device__ __forceinline__ const char* Abase(const pg8::Unit& u) const { size_t o = WS_R1; if (u.aux == 1) o = WS_R3; return ws + o + (size_t)u.pm * TSF8; }
;     __device__ __forceinline__ const char* Bbase(const pg8::Unit& u) const { size_t o = WS_WIN; if (u.aux == 1) o = WS_WKV; return ws + o + (size_t)u.pn * TSF8; }
;     __device__ __forceinline__ const char* Abase(const pg8::Unit& u) const { if (GATH) return ws + WS_XQ; return ws + WS_H2 + (size_t)u.pm * TSF8; }
; template <class Epi, class Sched, bool F8 = false, bool PF = false, bool I8 = false, int PID = -1>
; __device__ __forceinline__ void gemm_phase(LAS unsigned char* lds, LAS unsigned char* xlds, const int RP, const int RPB, const int nt, const Sched& S, const Epi& E, const int stagger_ticks) {
;     ...
;         cur = nxt; cA = nA; cB = nB; ++ui;
;         has_next = has_nn; nxt = nn;
;         if (has_next) { nA = PG8_UNI64(S.Abase(nxt)); nB = PG8_UNI64(S.Bbase(nxt)); }
;     __device__ __forceinline__ void operator()(const f32x4 (&acc)[2][2][4][2], const pg8::Unit& u, int wr, int wc, int fr, int fq) const {
;     ...
;         for (int ai = 0; ai < 2; ++ai)
; #pragma unroll
;             for (int m = 0; m < 4; ++m) { const int rl = ai * 128 + wr * 64 + m * 16 + fr;
;                 { const f32x4 v0 = acc[ai][0][m][0] * (1.0f / 64.0f) + bd[0][0], v1 = acc[ai][0][m][1] * (1.0f / 64.0f) + bd[0][1], v2 = acc[ai][1][m][0] * (1.0f / 64.0f) + bd[1][0], v3 = acc[ai][1][m][1] * (1.0f / 64.0f) + bd[1][1];
;                     *(u32x4*)(Yt + (size_t)rl * D + col0) = (u32x4){pk4_fp8(v0[0], v0[1], v0[2], v0[3]), pk4_fp8(v1[0], v1[1], v1[2], v1[3]), pk4_fp8(v2[0], v2[1], v2[2], v2[3]), pk4_fp8(v3[0], v3[1], v3[2], v3[3])}; } }
	v_cvt_pk_fp8_f32 v21, v30, v31 op_sel:[0,0,1]
	v_cvt_pk_fp8_f32 v22, v98, v99 op_sel:[0,0,1]
	v_cvt_pk_fp8_f32 v23, v102, v103 op_sel:[0,0,1]
	v_ashrrev_i32_e32 v25, 31, v24
	v_lshlrev_b64 v[24:25], 10, v[24:25]
	v_lshl_add_u64 v[24:25], v[26:27], 0, v[24:25]
	global_store_dwordx4 v[24:25], v[20:23], off
	v_pk_fma_f32 v[26:27], v[84:85], s[22:23], v[12:13] op_sel_hi:[1,0,1]
	v_pk_fma_f32 v[28:29], v[82:83], s[22:23], v[10:11] op_sel_hi:[1,0,1]
	v_pk_fma_f32 v[22:23], v[86:87], s[22:23], v[14:15] op_sel_hi:[1,0,1]
	v_mov_b32_e32 v20, 0
	v_pk_fma_f32 v[32:33], v[94:95], s[22:23], v[6:7] op_sel_hi:[1,0,1]
	v_pk_fma_f32 v[84:85], v[90:91], s[22:23], v[2:3] op_sel_hi:[1,0,1]
	v_cvt_pk_fp8_f32 v20, v22, v23
	v_mov_b32_e32 v21, 0
	v_mov_b32_e32 v22, 0
	v_mov_b32_e32 v23, 0
	v_cvt_pk_fp8_f32 v21, v28, v29
	v_cvt_pk_fp8_f32 v22, v32, v33
	v_cvt_pk_fp8_f32 v23, v84, v85
	v_pk_fma_f32 v[24:25], v[88:89], s[22:23], v[16:17] op_sel_hi:[1,0,1]
	v_pk_fma_f32 v[30:31], v[96:97], s[22:23], v[8:9] op_sel_hi:[1,0,1]
	v_pk_fma_f32 v[82:83], v[92:93], s[22:23], v[4:5] op_sel_hi:[1,0,1]
	v_cvt_pk_fp8_f32 v20, v24, v25 op_sel:[0,0,1]
	v_cvt_pk_fp8_f32 v21, v26, v27 op_sel:[0,0,1]
	v_cvt_pk_fp8_f32 v22, v30, v31 op_sel:[0,0,1]
	v_cvt_pk_fp8_f32 v23, v82, v83 op_sel:[0,0,1]
	v_add_co_u32_e32 v24, vcc, s67, v18
	v_pk_fma_f32 v[26:27], v[68:69], s[22:23], v[12:13] op_sel_hi:[1,0,1]
	s_nop 0
	v_addc_co_u32_e32 v25, vcc, 0, v19, vcc
	global_store_dwordx4 v[24:25], v[20:23], off
	v_pk_fma_f32 v[28:29], v[66:67], s[22:23], v[10:11] op_sel_hi:[1,0,1]
	v_pk_fma_f32 v[32:33], v[78:79], s[22:23], v[6:7] op_sel_hi:[1,0,1]
	v_pk_fma_f32 v[22:23], v[70:71], s[22:23], v[14:15] op_sel_hi:[1,0,1]
	v_mov_b32_e32 v20, 0
	v_pk_fma_f32 v[68:69], v[74:75], s[22:23], v[2:3] op_sel_hi:[1,0,1]
	v_cvt_pk_fp8_f32 v20, v22, v23
	v_mov_b32_e32 v21, 0
	v_mov_b32_e32 v22, 0
	v_mov_b32_e32 v23, 0
	v_cvt_pk_fp8_f32 v21, v28, v29
	v_cvt_pk_fp8_f32 v22, v32, v33
	v_cvt_pk_fp8_f32 v23, v68, v69
	v_pk_fma_f32 v[24:25], v[72:73], s[22:23], v[16:17] op_sel_hi:[1,0,1]
	v_pk_fma_f32 v[30:31], v[80:81], s[22:23], v[8:9] op_sel_hi:[1,0,1]
	v_pk_fma_f32 v[66:67], v[76:77], s[22:23], v[4:5] op_sel_hi:[1,0,1]
	v_cvt_pk_fp8_f32 v20, v24, v25 op_sel:[0,0,1]
	v_cvt_pk_fp8_f32 v21, v26, v27 op_sel:[0,0,1]
	v_cvt_pk_fp8_f32 v22, v30, v31 op_sel:[0,0,1]
	v_cvt_pk_fp8_f32 v23, v66, v67 op_sel:[0,0,1]
	v_add_co_u32_e32 v24, vcc, s68, v18
	v_pk_fma_f32 v[26:27], v[52:53], s[22:23], v[12:13] op_sel_hi:[1,0,1]
	s_nop 0
	v_addc_co_u32_e32 v25, vcc, 0, v19, vcc
	global_store_dwordx4 v[24:25], v[20:23], off
	v_pk_fma_f32 v[28:29], v[50:51], s[22:23], v[10:11] op_sel_hi:[1,0,1]
	v_pk_fma_f32 v[32:33], v[62:63], s[22:23], v[6:7] op_sel_hi:[1,0,1]
	v_pk_fma_f32 v[22:23], v[54:55], s[22:23], v[14:15] op_sel_hi:[1,0,1]
	v_mov_b32_e32 v20, 0
	v_pk_fma_f32 v[52:53], v[58:59], s[22:23], v[2:3] op_sel_hi:[1,0,1]
	v_cvt_pk_fp8_f32 v20, v22, v23
	v_mov_b32_e32 v21, 0
	v_mov_b32_e32 v22, 0
	v_mov_b32_e32 v23, 0
	v_cvt_pk_fp8_f32 v21, v28, v29
	v_cvt_pk_fp8_f32 v22, v32, v33
	v_cvt_pk_fp8_f32 v23, v52, v53
	v_pk_fma_f32 v[24:25], v[56:57], s[22:23], v[16:17] op_sel_hi:[1,0,1]
	v_pk_fma_f32 v[30:31], v[64:65], s[22:23], v[8:9] op_sel_hi:[1,0,1]
	v_pk_fma_f32 v[50:51], v[60:61], s[22:23], v[4:5] op_sel_hi:[1,0,1]
	v_cvt_pk_fp8_f32 v20, v24, v25 op_sel:[0,0,1]
	v_cvt_pk_fp8_f32 v21, v26, v27 op_sel:[0,0,1]
	v_cvt_pk_fp8_f32 v22, v30, v31 op_sel:[0,0,1]
	v_cvt_pk_fp8_f32 v23, v50, v51 op_sel:[0,0,1]
	v_add_co_u32_e32 v24, vcc, s69, v18
	v_pk_fma_f32 v[14:15], v[38:39], s[22:23], v[14:15] op_sel_hi:[1,0,1]
	s_nop 0
	v_addc_co_u32_e32 v25, vcc, 0, v19, vcc
	global_store_dwordx4 v[24:25], v[20:23], off
	v_pk_fma_f32 v[10:11], v[34:35], s[22:23], v[10:11] op_sel_hi:[1,0,1]
	v_pk_fma_f32 v[6:7], v[46:47], s[22:23], v[6:7] op_sel_hi:[1,0,1]
	v_pk_fma_f32 v[20:21], v[44:45], s[22:23], v[4:5] op_sel_hi:[1,0,1]
	v_pk_fma_f32 v[22:23], v[42:43], s[22:23], v[2:3] op_sel_hi:[1,0,1]
	v_mov_b32_e32 v2, 0
	v_mov_b32_e32 v3, 0
	v_mov_b32_e32 v4, 0
	v_mov_b32_e32 v5, 0
	v_cvt_pk_fp8_f32 v2, v14, v15
	v_cvt_pk_fp8_f32 v3, v10, v11
	v_cvt_pk_fp8_f32 v4, v6, v7
	v_cvt_pk_fp8_f32 v5, v22, v23
	v_pk_fma_f32 v[16:17], v[40:41], s[22:23], v[16:17] op_sel_hi:[1,0,1]
	v_pk_fma_f32 v[12:13], v[36:37], s[22:23], v[12:13] op_sel_hi:[1,0,1]
	v_pk_fma_f32 v[8:9], v[48:49], s[22:23], v[8:9] op_sel_hi:[1,0,1]
	v_cvt_pk_fp8_f32 v2, v16, v17 op_sel:[0,0,1]
	v_cvt_pk_fp8_f32 v3, v12, v13 op_sel:[0,0,1]
	v_cvt_pk_fp8_f32 v4, v8, v9 op_sel:[0,0,1]
	v_cvt_pk_fp8_f32 v5, v20, v21 op_sel:[0,0,1]
	v_add_co_u32_e32 v6, vcc, 0x2c000, v18
	s_mov_b64 s[26:27], -1
	s_nop 0
	v_addc_co_u32_e32 v7, vcc, 0, v19, vcc
	s_and_b64 vcc, exec, s[2:3]
	global_store_dwordx4 v[6:7], v[2:5], off
	s_cbranch_vccnz .LBB0_1060
	s_andn2_b64 vcc, exec, s[10:11]
	s_mov_b64 s[24:25], s[8:9]
	s_mov_b64 s[2:3], s[6:7]
	s_cbranch_vccnz .LBB0_1078
	s_ashr_i32 s15, s14, 31
	s_lshl_b64 s[2:3], s[14:15], 18
	s_add_u32 s2, s42, s2
	s_addc_u32 s3, s43, s3
	s_lshl_b32 s15, s46, 2
	s_add_i32 s24, s15, s5
	s_ashr_i32 s25, s24, 31
	s_lshl_b64 s[24:25], s[24:25], 18
	s_add_u32 s24, s44, s24
	s_addc_u32 s25, s45, s25
